# att3_kburst_after_barrier
# baseline (speedup 1.0000x reference)
; __device__ __forceinline__ void qkt64c(f32x16& p0, f32x16& p1, const char* Ks, const bf16x8* qr, const f32x16& cinit, int r32, int hi) {
; #pragma unroll
;     for (int d0 = 0; d0 < 4; ++d0) { const int cb = (d0 * 16 + hi * 8) * 2;
;         const bf16x8 b0 = *reinterpret_cast<const bf16x8*>(Ks + kswz<64>(r32, cb));
;         const bf16x8 b1 = *reinterpret_cast<const bf16x8*>(Ks + kswz<64>(32 + r32, cb));
;         if (d0 == 0) { p0 = __builtin_amdgcn_mfma_f32_32x32x16_bf16(b0, qr[0], cinit, 0, 0, 0); p1 = __builtin_amdgcn_mfma_f32_32x32x16_bf16(b1, qr[0], cinit, 0, 0, 0); }
;         else { p0 = __builtin_amdgcn_mfma_f32_32x32x16_bf16(b0, qr[d0], p0, 0, 0, 0); p1 = __builtin_amdgcn_mfma_f32_32x32x16_bf16(b1, qr[d0], p1, 0, 0, 0); } }
; }
.LBB0_823:
	s_lshl_b32 s2, s42, 13
	s_add_i32 s2, s2, 0
	v_add_u32_e32 v128, s2, v223
	ds_read_b128 v[144:147], v128 offset:49152
	v_add_u32_e32 v129, s2, v226
	ds_read_b128 v[148:151], v129 offset:49152
	v_add_u32_e32 v130, s2, v228
	ds_read_b128 v[152:155], v130 offset:49152
	v_add_u32_e32 v131, s2, v229
	ds_read_b128 v[156:159], v131 offset:49152
	ds_read_b128 v[232:235], v128 offset:53248
	ds_read_b128 v[236:239], v129 offset:53248
	ds_read_b128 v[240:243], v130 offset:53248
	ds_read_b128 v[244:247], v131 offset:53248
	v_lshl_add_u64 v[202:203], v[200:201], 0, s[64:65]
	s_mov_b32 s2, 0x8a40000
	v_add_co_u32_e32 v64, vcc, s2, v202
	s_mov_b32 s2, 0x8a50000
	s_nop 0
	v_addc_co_u32_e32 v65, vcc, 0, v203, vcc
	v_add_co_u32_e32 v66, vcc, s2, v202
	v_lshl_add_u64 v[204:205], v[198:199], 0, s[64:65]
	s_nop 0
	v_addc_co_u32_e32 v67, vcc, 0, v203, vcc
	s_mov_b32 s2, 0x6a40000
	global_load_dwordx4 v[178:181], v[64:65], off
	global_load_dwordx4 v[182:185], v[66:67], off
	v_add_co_u32_e32 v64, vcc, s2, v204
	s_nop 1
	v_addc_co_u32_e32 v65, vcc, 0, v205, vcc
	global_load_dwordx4 v[186:189], v[64:65], off
	v_exp_f32_e32 v190, v120
	v_exp_f32_e32 v191, v121
	v_add_f32_e32 v120, v96, v97
	v_add_f32_e32 v121, v98, v99
	s_waitcnt lgkmcnt(7)
	v_mfma_f32_32x32x16_bf16 v[128:143], v[144:147], v[162:165], v[80:95]
	v_exp_f32_e32 v192, v122
	v_add_f32_e32 v120, v120, v121
	v_add_f32_e32 v121, v100, v101
	v_add_f32_e32 v122, v102, v103
	v_exp_f32_e32 v193, v123
	s_waitcnt lgkmcnt(6)
	v_mfma_f32_32x32x16_bf16 v[128:143], v[148:151], v[166:169], v[128:143]
	v_add_f32_e32 v121, v121, v122
	v_add_f32_e32 v122, v104, v105
	v_add_f32_e32 v123, v106, v107
	v_add_f32_e32 v122, v122, v123
	v_add_f32_e32 v123, v108, v109
	s_waitcnt lgkmcnt(5)
	v_mfma_f32_32x32x16_bf16 v[128:143], v[152:155], v[170:173], v[128:143]
	v_add_f32_e32 v208, v110, v111
	v_add_f32_e32 v123, v123, v208
	v_add_f32_e32 v208, v112, v113
	v_add_f32_e32 v209, v114, v115
	v_add_f32_e32 v208, v208, v209
	s_waitcnt lgkmcnt(4)
	v_mfma_f32_32x32x16_bf16 v[128:143], v[156:159], v[174:177], v[128:143]
	v_exp_f32_e32 v124, v124
	v_exp_f32_e32 v125, v125
	s_waitcnt lgkmcnt(3)
	v_mfma_f32_32x32x16_bf16 v[144:159], v[232:235], v[162:165], v[80:95]
	v_exp_f32_e32 v126, v126
	v_exp_f32_e32 v127, v127
	v_add_f32_e32 v120, v208, v120
	v_add_f32_e32 v208, v116, v117
	v_add_f32_e32 v209, v118, v119
	v_add_f32_e32 v208, v208, v209
	v_add_f32_e32 v121, v208, v121
	s_waitcnt lgkmcnt(2)
	v_mfma_f32_32x32x16_bf16 v[144:159], v[236:239], v[166:169], v[144:159]
	v_add_f32_e32 v208, v190, v191
	v_add_f32_e32 v209, v192, v193
	v_add_f32_e32 v208, v208, v209
	v_add_f32_e32 v122, v122, v208
	v_add_f32_e32 v208, v124, v125
	v_add_f32_e32 v209, v126, v127
	v_add_f32_e32 v208, v208, v209
	s_waitcnt lgkmcnt(1)
	v_mfma_f32_32x32x16_bf16 v[144:159], v[240:243], v[170:173], v[144:159]
	v_add_f32_e32 v123, v123, v208
	v_add_f32_e32 v120, v120, v121
	v_add_f32_e32 v121, v122, v123
	v_add_f32_e32 v231, v120, v121
	v_mov_b32_e32 v232, v231
	v_cvt_pk_bf16_f32 v96, v96, v97
	v_cvt_pk_bf16_f32 v97, v98, v99
	s_waitcnt lgkmcnt(0)
	v_mfma_f32_32x32x16_bf16 v[144:159], v[244:247], v[174:177], v[144:159]
	v_cvt_pk_bf16_f32 v98, v100, v101
	v_cvt_pk_bf16_f32 v99, v102, v103
	v_cvt_pk_bf16_f32 v120, v104, v105
	v_cvt_pk_bf16_f32 v121, v106, v107
	v_cvt_pk_bf16_f32 v122, v108, v109
	v_cvt_pk_bf16_f32 v123, v110, v111
	v_cvt_pk_bf16_f32 v104, v112, v113
	v_cvt_pk_bf16_f32 v105, v114, v115
	v_cvt_pk_bf16_f32 v106, v116, v117
	v_cvt_pk_bf16_f32 v107, v118, v119
	v_cvt_pk_bf16_f32 v100, v190, v191
	v_cvt_pk_bf16_f32 v101, v192, v193
	v_cvt_pk_bf16_f32 v102, v124, v125
	v_cvt_pk_bf16_f32 v103, v126, v127
	s_nop 0
	v_permlane32_swap_b32_e32 v231, v232
	v_permlane32_swap_b32_e32 v96, v98
	v_permlane32_swap_b32_e32 v97, v99
	v_permlane32_swap_b32_e32 v120, v122
	v_permlane32_swap_b32_e32 v121, v123
	v_permlane32_swap_b32_e32 v104, v106
	v_permlane32_swap_b32_e32 v105, v107
	v_permlane32_swap_b32_e32 v100, v102
	v_permlane32_swap_b32_e32 v101, v103
	v_lshl_add_u32 v234, s12, 14, v217
	ds_read_b64_tr_b16 v[108:109], v234 offset:0
	ds_read_b64_tr_b16 v[110:111], v234 offset:0x800
	ds_read_b64_tr_b16 v[112:113], v234 offset:0x1000
	ds_read_b64_tr_b16 v[114:115], v234 offset:0x1800
	ds_read_b64_tr_b16 v[116:117], v234 offset:0x2000
	ds_read_b64_tr_b16 v[118:119], v234 offset:0x2800
	ds_read_b64_tr_b16 v[124:125], v234 offset:0x3000
	ds_read_b64_tr_b16 v[126:127], v234 offset:0x3800
	ds_read_b64_tr_b16 v[236:237], v234 offset:0x200
	ds_read_b64_tr_b16 v[238:239], v234 offset:0xa00
	ds_read_b64_tr_b16 v[240:241], v234 offset:0x1200
	ds_read_b64_tr_b16 v[242:243], v234 offset:0x1a00
	ds_read_b64_tr_b16 v[244:245], v234 offset:0x2200
	ds_read_b64_tr_b16 v[246:247], v234 offset:0x2a00
	ds_read_b64_tr_b16 v[190:191], v234 offset:0x3200
	ds_read_b64_tr_b16 v[192:193], v234 offset:0x3a00
	s_waitcnt lgkmcnt(8)
	s_nop 0
	v_mfma_f32_32x32x16_bf16 v[0:15], v[96:99], v[108:111], v[0:15]
	v_max_f32_e32 v108, v128, v129
	v_max3_f32 v109, v130, v131, v145
	v_max3_f32 v108, v108, v144, v146
	v_max3_f32 v108, v108, v147, v132
	v_max3_f32 v109, v109, v134, v135
	v_mfma_f32_32x32x16_bf16 v[0:15], v[120:123], v[112:115], v[0:15]
	v_max3_f32 v208, v108, v133, v148
	v_max3_f32 v209, v109, v150, v151
	v_mfma_f32_32x32x16_bf16 v[0:15], v[104:107], v[116:119], v[0:15]
	v_mfma_f32_32x32x16_bf16 v[0:15], v[100:103], v[124:127], v[0:15]
	ds_read_b64_tr_b16 v[124:125], v234 offset:0x400
	ds_read_b64_tr_b16 v[126:127], v234 offset:0xc00
	ds_read_b64_tr_b16 v[116:117], v234 offset:0x1400
	ds_read_b64_tr_b16 v[118:119], v234 offset:0x1c00
	ds_read_b64_tr_b16 v[112:113], v234 offset:0x2400
	ds_read_b64_tr_b16 v[114:115], v234 offset:0x2c00
	ds_read_b64_tr_b16 v[108:109], v234 offset:0x3400
	ds_read_b64_tr_b16 v[110:111], v234 offset:0x3c00
	s_waitcnt lgkmcnt(8)
	v_mfma_f32_32x32x16_bf16 v[48:63], v[96:99], v[236:239], v[48:63]
	v_max3_f32 v208, v208, v149, v136
	v_max3_f32 v209, v209, v138, v139
	v_max3_f32 v208, v208, v137, v152
	v_max3_f32 v209, v209, v154, v155
	v_max3_f32 v208, v208, v153, v140
	v_max3_f32 v209, v209, v142, v143
	v_max3_f32 v208, v208, v141, v156
	v_mfma_f32_32x32x16_bf16 v[48:63], v[120:123], v[240:243], v[48:63]
	v_max3_f32 v209, v209, v158, v159
	v_max3_f32 v208, v208, v157, v209
	v_mov_b32_e32 v209, v208
	s_nop 1
	v_permlane32_swap_b32_e32 v208, v209
	v_mfma_f32_32x32x16_bf16 v[48:63], v[104:107], v[244:247], v[48:63]
	v_max_f32_e32 v233, v208, v209
	v_mfma_f32_32x32x16_bf16 v[48:63], v[100:103], v[190:193], v[48:63]
	s_mov_b32 s2, 0x4138aa3b
	v_cmp_ge_f32_e32 vcc, s2, v233
	s_cmp_eq_u64 vcc, exec
	s_cbranch_scc0 .LBB0_836
	v_mov_b32_e32 v233, 1.0

; __device__ __forceinline__ void qkt64c(f32x16& p0, f32x16& p1, const char* Ks, const bf16x8* qr, const f32x16& cinit, int r32, int hi) {
; #pragma unroll
;     for (int d0 = 0; d0 < 4; ++d0) { const int cb = (d0 * 16 + hi * 8) * 2;
;         const bf16x8 b0 = *reinterpret_cast<const bf16x8*>(Ks + kswz<64>(r32, cb));
;         const bf16x8 b1 = *reinterpret_cast<const bf16x8*>(Ks + kswz<64>(32 + r32, cb));
;         if (d0 == 0) { p0 = __builtin_amdgcn_mfma_f32_32x32x16_bf16(b0, qr[0], cinit, 0, 0, 0); p1 = __builtin_amdgcn_mfma_f32_32x32x16_bf16(b1, qr[0], cinit, 0, 0, 0); }
;         else { p0 = __builtin_amdgcn_mfma_f32_32x32x16_bf16(b0, qr[d0], p0, 0, 0, 0); p1 = __builtin_amdgcn_mfma_f32_32x32x16_bf16(b1, qr[d0], p1, 0, 0, 0); } }
; }
.LBB0_829:
	v_add_co_u32_e32 v96, vcc, 0x8a60000, v202
	s_waitcnt lgkmcnt(0)
	s_nop 0
	v_addc_co_u32_e32 v97, vcc, 0, v203, vcc
	v_add_co_u32_e32 v98, vcc, 0x8a70000, v202
	s_nop 1
	v_addc_co_u32_e32 v99, vcc, 0, v203, vcc
	v_add_co_u32_e32 v100, vcc, 0x6a60000, v204
	s_nop 1
	v_addc_co_u32_e32 v101, vcc, 0, v205, vcc
	s_barrier
	v_add_u32_e32 v102, s2, v223
	ds_read_b128 v[112:115], v102 offset:49152
	v_add_u32_e32 v103, s2, v226
	ds_read_b128 v[116:119], v103 offset:49152
	v_add_u32_e32 v104, s2, v228
	ds_read_b128 v[120:123], v104 offset:49152
	v_add_u32_e32 v105, s2, v229
	ds_read_b128 v[124:127], v105 offset:49152
	ds_read_b128 v[190:193], v102 offset:53248
	ds_read_b128 v[202:205], v103 offset:53248
	ds_read_b128 v[234:237], v104 offset:53248
	ds_read_b128 v[238:241], v105 offset:53248
	global_load_dwordx4 v[178:181], v[96:97], off
	global_load_dwordx4 v[182:185], v[98:99], off
	global_load_dwordx4 v[186:189], v[100:101], off
	v_exp_f32_e32 v208, v152
	v_exp_f32_e32 v209, v153
	v_add_f32_e32 v152, v128, v129
	v_add_f32_e32 v153, v130, v131
	s_waitcnt lgkmcnt(7)
	v_mfma_f32_32x32x16_bf16 v[96:111], v[112:115], v[162:165], v[80:95]
	v_exp_f32_e32 v210, v154
	v_add_f32_e32 v152, v152, v153
	v_add_f32_e32 v153, v132, v133
	v_add_f32_e32 v154, v134, v135
	v_exp_f32_e32 v211, v155
	s_waitcnt lgkmcnt(6)
	v_mfma_f32_32x32x16_bf16 v[96:111], v[116:119], v[166:169], v[96:111]
	v_add_f32_e32 v153, v153, v154
	v_add_f32_e32 v154, v136, v137
	v_add_f32_e32 v155, v138, v139
	v_add_f32_e32 v154, v154, v155
	v_add_f32_e32 v155, v140, v141
	s_waitcnt lgkmcnt(5)
	v_mfma_f32_32x32x16_bf16 v[96:111], v[120:123], v[170:173], v[96:111]
	v_exp_f32_e32 v156, v156
	v_exp_f32_e32 v157, v157
	v_exp_f32_e32 v158, v158
	v_exp_f32_e32 v159, v159
	s_waitcnt lgkmcnt(4)
	v_mfma_f32_32x32x16_bf16 v[96:111], v[124:127], v[174:177], v[96:111]
	s_waitcnt lgkmcnt(3)
	v_mfma_f32_32x32x16_bf16 v[112:127], v[190:193], v[162:165], v[80:95]
	v_add_f32_e32 v190, v142, v143
	v_add_f32_e32 v155, v155, v190
	v_add_f32_e32 v190, v144, v145
	v_add_f32_e32 v191, v146, v147
	v_add_f32_e32 v190, v190, v191
	v_add_f32_e32 v152, v152, v190
	v_add_f32_e32 v190, v148, v149
	s_waitcnt lgkmcnt(2)
	v_mfma_f32_32x32x16_bf16 v[112:127], v[202:205], v[166:169], v[112:127]
	v_add_f32_e32 v191, v150, v151
	v_add_f32_e32 v190, v190, v191
	v_add_f32_e32 v153, v153, v190
	v_add_f32_e32 v190, v208, v209
	v_add_f32_e32 v191, v210, v211
	v_add_f32_e32 v190, v190, v191
	v_add_f32_e32 v154, v154, v190
	s_waitcnt lgkmcnt(1)
	v_mfma_f32_32x32x16_bf16 v[112:127], v[234:237], v[170:173], v[112:127]
	v_add_f32_e32 v190, v156, v157
	v_add_f32_e32 v191, v158, v159
	v_add_f32_e32 v190, v190, v191
	v_add_f32_e32 v155, v155, v190
	v_add_f32_e32 v152, v152, v153
	v_add_f32_e32 v153, v154, v155
	v_add_f32_e32 v203, v152, v153
	s_waitcnt lgkmcnt(0)
	v_mfma_f32_32x32x16_bf16 v[112:127], v[238:241], v[174:177], v[112:127]
	v_mov_b32_e32 v204, v203
	v_cvt_pk_bf16_f32 v152, v128, v129
	v_cvt_pk_bf16_f32 v153, v130, v131
	v_cvt_pk_bf16_f32 v154, v132, v133
	v_cvt_pk_bf16_f32 v155, v134, v135
	v_cvt_pk_bf16_f32 v136, v136, v137
	v_cvt_pk_bf16_f32 v137, v138, v139
	v_cvt_pk_bf16_f32 v138, v140, v141
	v_cvt_pk_bf16_f32 v139, v142, v143
	v_cvt_pk_bf16_f32 v132, v144, v145
	v_cvt_pk_bf16_f32 v133, v146, v147
	v_cvt_pk_bf16_f32 v134, v148, v149
	v_cvt_pk_bf16_f32 v135, v150, v151
	v_cvt_pk_bf16_f32 v128, v208, v209
	v_cvt_pk_bf16_f32 v129, v210, v211
	v_cvt_pk_bf16_f32 v130, v156, v157
	v_cvt_pk_bf16_f32 v131, v158, v159
	s_nop 1
	v_permlane32_swap_b32_e32 v203, v204
	v_permlane32_swap_b32_e32 v152, v154
	v_permlane32_swap_b32_e32 v153, v155
	v_permlane32_swap_b32_e32 v136, v138
	v_permlane32_swap_b32_e32 v137, v139
	v_permlane32_swap_b32_e32 v132, v134
	v_permlane32_swap_b32_e32 v133, v135
	v_permlane32_swap_b32_e32 v128, v130
	v_permlane32_swap_b32_e32 v129, v131
	v_lshl_add_u32 v205, s42, 14, v217
	ds_read_b64_tr_b16 v[140:141], v205 offset:0
	ds_read_b64_tr_b16 v[142:143], v205 offset:0x800
	ds_read_b64_tr_b16 v[144:145], v205 offset:0x1000
	ds_read_b64_tr_b16 v[146:147], v205 offset:0x1800
	ds_read_b64_tr_b16 v[148:149], v205 offset:0x2000
	ds_read_b64_tr_b16 v[150:151], v205 offset:0x2800
	ds_read_b64_tr_b16 v[156:157], v205 offset:0x3000
	ds_read_b64_tr_b16 v[158:159], v205 offset:0x3800
	ds_read_b64_tr_b16 v[190:191], v205 offset:0x200
	ds_read_b64_tr_b16 v[192:193], v205 offset:0xa00
	ds_read_b64_tr_b16 v[234:235], v205 offset:0x1200
	ds_read_b64_tr_b16 v[236:237], v205 offset:0x1a00
	ds_read_b64_tr_b16 v[238:239], v205 offset:0x2200
	ds_read_b64_tr_b16 v[240:241], v205 offset:0x2a00
	ds_read_b64_tr_b16 v[242:243], v205 offset:0x3200
	ds_read_b64_tr_b16 v[244:245], v205 offset:0x3a00
	s_waitcnt lgkmcnt(8)
	s_nop 0
	v_mfma_f32_32x32x16_bf16 v[0:15], v[152:155], v[140:143], v[0:15]
	v_max_f32_e32 v140, v96, v97
	v_max3_f32 v140, v140, v112, v114
	v_max3_f32 v141, v98, v99, v113
	v_max3_f32 v140, v140, v115, v100
	v_max3_f32 v141, v141, v102, v103
	v_mfma_f32_32x32x16_bf16 v[0:15], v[136:139], v[144:147], v[0:15]
	v_max3_f32 v202, v140, v101, v116
	v_max3_f32 v208, v141, v118, v119
	v_mfma_f32_32x32x16_bf16 v[0:15], v[132:135], v[148:151], v[0:15]
	v_mfma_f32_32x32x16_bf16 v[0:15], v[128:131], v[156:159], v[0:15]
	ds_read_b64_tr_b16 v[156:157], v205 offset:0x400
	ds_read_b64_tr_b16 v[158:159], v205 offset:0xc00
	ds_read_b64_tr_b16 v[148:149], v205 offset:0x1400
	ds_read_b64_tr_b16 v[150:151], v205 offset:0x1c00
	ds_read_b64_tr_b16 v[144:145], v205 offset:0x2400
	ds_read_b64_tr_b16 v[146:147], v205 offset:0x2c00
	ds_read_b64_tr_b16 v[140:141], v205 offset:0x3400
	ds_read_b64_tr_b16 v[142:143], v205 offset:0x3c00
	s_waitcnt lgkmcnt(8)
	v_mfma_f32_32x32x16_bf16 v[48:63], v[152:155], v[190:193], v[48:63]
	v_max3_f32 v190, v202, v117, v104
	v_max3_f32 v191, v208, v106, v107
	v_max3_f32 v190, v190, v105, v120
	v_max3_f32 v191, v191, v122, v123
	v_max3_f32 v190, v190, v121, v108
	v_max3_f32 v191, v191, v110, v111
	v_max3_f32 v190, v190, v109, v124
	v_mfma_f32_32x32x16_bf16 v[48:63], v[136:139], v[234:237], v[48:63]
	v_max3_f32 v191, v191, v126, v127
	v_max3_f32 v190, v190, v125, v191
	v_mov_b32_e32 v191, v190
	s_nop 1
	v_permlane32_swap_b32_e32 v190, v191
	v_mfma_f32_32x32x16_bf16 v[48:63], v[132:135], v[238:241], v[48:63]
	v_max_f32_e32 v234, v190, v191
	v_mfma_f32_32x32x16_bf16 v[48:63], v[128:131], v[242:245], v[48:63]
	s_mov_b32 s2, 0x4138aa3b
	v_cmp_ge_f32_e32 vcc, s2, v234
	s_cmp_eq_u64 vcc, exec
	v_mov_b32_e32 v202, 1.0
	s_cbranch_scc0 .LBB0_837

; __device__ __forceinline__ void qkt64c(f32x16& p0, f32x16& p1, const char* Ks, const bf16x8* qr, const f32x16& cinit, int r32, int hi) {
; #pragma unroll
;     for (int d0 = 0; d0 < 4; ++d0) { const int cb = (d0 * 16 + hi * 8) * 2;
;         const bf16x8 b0 = *reinterpret_cast<const bf16x8*>(Ks + kswz<64>(r32, cb));
;         const bf16x8 b1 = *reinterpret_cast<const bf16x8*>(Ks + kswz<64>(32 + r32, cb));
;         if (d0 == 0) { p0 = __builtin_amdgcn_mfma_f32_32x32x16_bf16(b0, qr[0], cinit, 0, 0, 0); p1 = __builtin_amdgcn_mfma_f32_32x32x16_bf16(b1, qr[0], cinit, 0, 0, 0); }
;         else { p0 = __builtin_amdgcn_mfma_f32_32x32x16_bf16(b0, qr[d0], p0, 0, 0, 0); p1 = __builtin_amdgcn_mfma_f32_32x32x16_bf16(b1, qr[d0], p1, 0, 0, 0); } }
; }
.LBB0_846:
	s_lshl_b32 s2, s30, 13
	s_add_i32 s2, s2, 0
	v_add_u32_e32 v128, s2, v227
	ds_read_b128 v[144:147], v128 offset:49152
	v_add_u32_e32 v129, s2, v231
	ds_read_b128 v[148:151], v129 offset:49152
	v_add_u32_e32 v130, s2, v232
	ds_read_b128 v[152:155], v130 offset:49152
	v_add_u32_e32 v131, s2, v233
	ds_read_b128 v[156:159], v131 offset:49152
	ds_read_b128 v[190:193], v128 offset:53248
	ds_read_b128 v[236:239], v129 offset:53248
	ds_read_b128 v[240:243], v130 offset:53248
	ds_read_b128 v[244:247], v131 offset:53248
	v_lshl_add_u64 v[202:203], v[200:201], 0, s[64:65]
	s_mov_b32 s2, 0x8a40000
	v_add_co_u32_e32 v64, vcc, s2, v202
	s_mov_b32 s2, 0x8a50000
	s_nop 0
	v_addc_co_u32_e32 v65, vcc, 0, v203, vcc
	v_add_co_u32_e32 v66, vcc, s2, v202
	v_lshl_add_u64 v[204:205], v[198:199], 0, s[64:65]
	s_nop 0
	v_addc_co_u32_e32 v67, vcc, 0, v203, vcc
	s_mov_b32 s2, 0x6a40000
	global_load_dwordx4 v[178:181], v[64:65], off
	global_load_dwordx4 v[182:185], v[66:67], off
	v_add_co_u32_e32 v64, vcc, s2, v204
	s_nop 1
	v_addc_co_u32_e32 v65, vcc, 0, v205, vcc
	global_load_dwordx4 v[186:189], v[64:65], off offset:128
	v_exp_f32_e32 v208, v120
	v_exp_f32_e32 v209, v121
	v_add_f32_e32 v120, v96, v97
	v_add_f32_e32 v121, v98, v99
	s_waitcnt lgkmcnt(7)
	v_mfma_f32_32x32x16_bf16 v[128:143], v[144:147], v[162:165], v[80:95]
	v_exp_f32_e32 v210, v122
	v_add_f32_e32 v120, v120, v121
	v_add_f32_e32 v121, v100, v101
	v_add_f32_e32 v122, v102, v103
	v_exp_f32_e32 v211, v123
	s_waitcnt lgkmcnt(6)
	v_mfma_f32_32x32x16_bf16 v[128:143], v[148:151], v[166:169], v[128:143]
	v_add_f32_e32 v121, v121, v122
	v_add_f32_e32 v122, v104, v105
	v_add_f32_e32 v123, v106, v107
	v_add_f32_e32 v122, v122, v123
	v_add_f32_e32 v123, v108, v109
	s_waitcnt lgkmcnt(5)
	v_mfma_f32_32x32x16_bf16 v[128:143], v[152:155], v[170:173], v[128:143]
	v_exp_f32_e32 v124, v124
	v_exp_f32_e32 v125, v125
	v_exp_f32_e32 v126, v126
	v_exp_f32_e32 v127, v127
	v_cvt_pk_bf16_f32 v96, v96, v97
	s_waitcnt lgkmcnt(4)
	v_mfma_f32_32x32x16_bf16 v[128:143], v[156:159], v[174:177], v[128:143]
	v_cvt_pk_bf16_f32 v97, v98, v99
	v_cvt_pk_bf16_f32 v98, v100, v101
	v_cvt_pk_bf16_f32 v99, v102, v103
	s_nop 0
	v_permlane32_swap_b32_e32 v96, v98
	s_waitcnt lgkmcnt(3)
	v_mfma_f32_32x32x16_bf16 v[144:159], v[190:193], v[162:165], v[80:95]
	v_add_f32_e32 v190, v110, v111
	v_add_f32_e32 v123, v123, v190
	v_add_f32_e32 v190, v112, v113
	v_add_f32_e32 v191, v114, v115
	v_add_f32_e32 v190, v190, v191
	v_add_f32_e32 v120, v190, v120
	v_add_f32_e32 v190, v116, v117
	s_waitcnt lgkmcnt(2)
	v_mfma_f32_32x32x16_bf16 v[144:159], v[236:239], v[166:169], v[144:159]
	v_add_f32_e32 v191, v118, v119
	v_add_f32_e32 v190, v190, v191
	v_add_f32_e32 v121, v190, v121
	v_add_f32_e32 v190, v208, v209
	v_add_f32_e32 v191, v210, v211
	v_add_f32_e32 v190, v190, v191
	v_add_f32_e32 v122, v122, v190
	s_waitcnt lgkmcnt(1)
	v_mfma_f32_32x32x16_bf16 v[144:159], v[240:243], v[170:173], v[144:159]
	v_add_f32_e32 v190, v124, v125
	v_add_f32_e32 v191, v126, v127
	v_add_f32_e32 v190, v190, v191
	v_add_f32_e32 v123, v123, v190
	v_add_f32_e32 v120, v120, v121
	v_add_f32_e32 v121, v122, v123
	v_add_f32_e32 v235, v120, v121
	s_waitcnt lgkmcnt(0)
	v_mfma_f32_32x32x16_bf16 v[144:159], v[244:247], v[174:177], v[144:159]
	v_mov_b32_e32 v236, v235
	v_cvt_pk_bf16_f32 v120, v104, v105
	v_cvt_pk_bf16_f32 v121, v106, v107
	v_cvt_pk_bf16_f32 v122, v108, v109
	v_cvt_pk_bf16_f32 v123, v110, v111
	v_cvt_pk_bf16_f32 v104, v112, v113
	v_cvt_pk_bf16_f32 v105, v114, v115
	v_cvt_pk_bf16_f32 v106, v116, v117
	v_cvt_pk_bf16_f32 v107, v118, v119
	v_cvt_pk_bf16_f32 v100, v208, v209
	v_cvt_pk_bf16_f32 v101, v210, v211
	v_cvt_pk_bf16_f32 v102, v124, v125
	v_cvt_pk_bf16_f32 v103, v126, v127
	s_nop 1
	v_permlane32_swap_b32_e32 v235, v236
	v_permlane32_swap_b32_e32 v97, v99
	v_permlane32_swap_b32_e32 v120, v122
	v_permlane32_swap_b32_e32 v121, v123
	v_permlane32_swap_b32_e32 v104, v106
	v_permlane32_swap_b32_e32 v105, v107
	v_permlane32_swap_b32_e32 v100, v102
	v_permlane32_swap_b32_e32 v101, v103
	v_lshl_add_u32 v238, s12, 14, v221
	ds_read_b64_tr_b16 v[108:109], v238 offset:0
	ds_read_b64_tr_b16 v[110:111], v238 offset:0x800
	ds_read_b64_tr_b16 v[112:113], v238 offset:0x1000
	ds_read_b64_tr_b16 v[114:115], v238 offset:0x1800
	ds_read_b64_tr_b16 v[116:117], v238 offset:0x2000
	ds_read_b64_tr_b16 v[118:119], v238 offset:0x2800
	ds_read_b64_tr_b16 v[124:125], v238 offset:0x3000
	ds_read_b64_tr_b16 v[126:127], v238 offset:0x3800
	ds_read_b64_tr_b16 v[190:191], v238 offset:0x200
	ds_read_b64_tr_b16 v[192:193], v238 offset:0xa00
	ds_read_b64_tr_b16 v[240:241], v238 offset:0x1200
	ds_read_b64_tr_b16 v[242:243], v238 offset:0x1a00
	ds_read_b64_tr_b16 v[244:245], v238 offset:0x2200
	ds_read_b64_tr_b16 v[246:247], v238 offset:0x2a00
	ds_read_b64_tr_b16 v[208:209], v238 offset:0x3200
	ds_read_b64_tr_b16 v[210:211], v238 offset:0x3a00
	s_waitcnt lgkmcnt(8)
	s_nop 0
	v_mfma_f32_32x32x16_bf16 v[0:15], v[96:99], v[108:111], v[0:15]
	v_max_f32_e32 v108, v128, v129
	v_max3_f32 v108, v108, v144, v146
	v_max3_f32 v109, v130, v131, v145
	v_max3_f32 v108, v108, v147, v132
	v_max3_f32 v109, v109, v134, v135
	v_mfma_f32_32x32x16_bf16 v[0:15], v[120:123], v[112:115], v[0:15]
	v_max3_f32 v237, v108, v133, v148
	v_max3_f32 v239, v109, v150, v151
	v_mfma_f32_32x32x16_bf16 v[0:15], v[104:107], v[116:119], v[0:15]
	v_mfma_f32_32x32x16_bf16 v[0:15], v[100:103], v[124:127], v[0:15]
	ds_read_b64_tr_b16 v[124:125], v238 offset:0x400
	ds_read_b64_tr_b16 v[126:127], v238 offset:0xc00
	ds_read_b64_tr_b16 v[116:117], v238 offset:0x1400
	ds_read_b64_tr_b16 v[118:119], v238 offset:0x1c00
	ds_read_b64_tr_b16 v[112:113], v238 offset:0x2400
	ds_read_b64_tr_b16 v[114:115], v238 offset:0x2c00
	ds_read_b64_tr_b16 v[108:109], v238 offset:0x3400
	ds_read_b64_tr_b16 v[110:111], v238 offset:0x3c00
	s_waitcnt lgkmcnt(8)
	v_mfma_f32_32x32x16_bf16 v[48:63], v[96:99], v[190:193], v[48:63]
	v_max3_f32 v190, v237, v149, v136
	v_max3_f32 v191, v239, v138, v139
	v_max3_f32 v190, v190, v137, v152
	v_max3_f32 v191, v191, v154, v155
	v_max3_f32 v190, v190, v153, v140
	v_max3_f32 v191, v191, v142, v143
	v_max3_f32 v190, v190, v141, v156
	v_mfma_f32_32x32x16_bf16 v[48:63], v[120:123], v[240:243], v[48:63]
	v_max3_f32 v191, v191, v158, v159
	v_max3_f32 v190, v190, v157, v191
	v_mov_b32_e32 v191, v190
	s_nop 1
	v_permlane32_swap_b32_e32 v190, v191
	v_mfma_f32_32x32x16_bf16 v[48:63], v[104:107], v[244:247], v[48:63]
	v_max_f32_e32 v237, v190, v191
	v_mfma_f32_32x32x16_bf16 v[48:63], v[100:103], v[208:211], v[48:63]
	s_mov_b32 s2, 0x4138aa3b
	v_cmp_ge_f32_e32 vcc, s2, v237
	s_cmp_eq_u64 vcc, exec
	s_cbranch_scc0 .LBB0_859
	v_mov_b32_e32 v237, 1.0

; __device__ __forceinline__ void qkt64c(f32x16& p0, f32x16& p1, const char* Ks, const bf16x8* qr, const f32x16& cinit, int r32, int hi) {
; #pragma unroll
;     for (int d0 = 0; d0 < 4; ++d0) { const int cb = (d0 * 16 + hi * 8) * 2;
;         const bf16x8 b0 = *reinterpret_cast<const bf16x8*>(Ks + kswz<64>(r32, cb));
;         const bf16x8 b1 = *reinterpret_cast<const bf16x8*>(Ks + kswz<64>(32 + r32, cb));
;         if (d0 == 0) { p0 = __builtin_amdgcn_mfma_f32_32x32x16_bf16(b0, qr[0], cinit, 0, 0, 0); p1 = __builtin_amdgcn_mfma_f32_32x32x16_bf16(b1, qr[0], cinit, 0, 0, 0); }
;         else { p0 = __builtin_amdgcn_mfma_f32_32x32x16_bf16(b0, qr[d0], p0, 0, 0, 0); p1 = __builtin_amdgcn_mfma_f32_32x32x16_bf16(b1, qr[d0], p1, 0, 0, 0); } }
; }
.LBB0_852:
	v_add_co_u32_e32 v96, vcc, 0x8a60000, v202
	s_waitcnt lgkmcnt(0)
	s_nop 0
	v_addc_co_u32_e32 v97, vcc, 0, v203, vcc
	v_add_co_u32_e32 v98, vcc, 0x8a70000, v202
	s_nop 1
	v_addc_co_u32_e32 v99, vcc, 0, v203, vcc
	v_add_co_u32_e32 v100, vcc, 0x6a60000, v204
	s_nop 1
	v_addc_co_u32_e32 v101, vcc, 0, v205, vcc
	s_barrier
	v_add_u32_e32 v102, s2, v227
	ds_read_b128 v[112:115], v102 offset:49152
	v_add_u32_e32 v103, s2, v231
	ds_read_b128 v[116:119], v103 offset:49152
	v_add_u32_e32 v104, s2, v232
	ds_read_b128 v[120:123], v104 offset:49152
	v_add_u32_e32 v105, s2, v233
	ds_read_b128 v[124:127], v105 offset:49152
	ds_read_b128 v[190:193], v102 offset:53248
	ds_read_b128 v[202:205], v103 offset:53248
	ds_read_b128 v[208:211], v104 offset:53248
	ds_read_b128 v[238:241], v105 offset:53248
	global_load_dwordx4 v[178:181], v[96:97], off
	global_load_dwordx4 v[182:185], v[98:99], off
	global_load_dwordx4 v[186:189], v[100:101], off offset:128
	v_exp_f32_e32 v242, v152
	v_exp_f32_e32 v243, v153
	v_add_f32_e32 v152, v128, v129
	v_add_f32_e32 v153, v130, v131
	s_waitcnt lgkmcnt(7)
	v_mfma_f32_32x32x16_bf16 v[96:111], v[112:115], v[162:165], v[80:95]
	v_exp_f32_e32 v244, v154
	v_add_f32_e32 v152, v152, v153
	v_add_f32_e32 v153, v132, v133
	v_add_f32_e32 v154, v134, v135
	v_exp_f32_e32 v245, v155
	s_waitcnt lgkmcnt(6)
	v_mfma_f32_32x32x16_bf16 v[96:111], v[116:119], v[166:169], v[96:111]
	v_add_f32_e32 v153, v153, v154
	v_add_f32_e32 v154, v136, v137
	v_add_f32_e32 v155, v138, v139
	v_add_f32_e32 v154, v154, v155
	v_add_f32_e32 v155, v140, v141
	s_waitcnt lgkmcnt(5)
	v_mfma_f32_32x32x16_bf16 v[96:111], v[120:123], v[170:173], v[96:111]
	v_exp_f32_e32 v156, v156
	v_exp_f32_e32 v157, v157
	v_exp_f32_e32 v158, v158
	v_exp_f32_e32 v159, v159
	s_waitcnt lgkmcnt(4)
	v_mfma_f32_32x32x16_bf16 v[96:111], v[124:127], v[174:177], v[96:111]
	s_waitcnt lgkmcnt(3)
	v_mfma_f32_32x32x16_bf16 v[112:127], v[190:193], v[162:165], v[80:95]
	v_add_f32_e32 v190, v142, v143
	v_add_f32_e32 v155, v155, v190
	v_add_f32_e32 v190, v144, v145
	v_add_f32_e32 v191, v146, v147
	v_add_f32_e32 v190, v190, v191
	v_add_f32_e32 v152, v152, v190
	v_add_f32_e32 v190, v148, v149
	s_waitcnt lgkmcnt(2)
	v_mfma_f32_32x32x16_bf16 v[112:127], v[202:205], v[166:169], v[112:127]
	v_add_f32_e32 v191, v150, v151
	v_add_f32_e32 v190, v190, v191
	v_add_f32_e32 v153, v153, v190
	v_add_f32_e32 v190, v242, v243
	v_add_f32_e32 v191, v244, v245
	v_add_f32_e32 v190, v190, v191
	v_add_f32_e32 v154, v154, v190
	s_waitcnt lgkmcnt(1)
	v_mfma_f32_32x32x16_bf16 v[112:127], v[208:211], v[170:173], v[112:127]
	v_add_f32_e32 v190, v156, v157
	v_add_f32_e32 v191, v158, v159
	v_add_f32_e32 v190, v190, v191
	v_add_f32_e32 v155, v155, v190
	v_add_f32_e32 v152, v152, v153
	v_add_f32_e32 v153, v154, v155
	v_add_f32_e32 v203, v152, v153
	s_waitcnt lgkmcnt(0)
	v_mfma_f32_32x32x16_bf16 v[112:127], v[238:241], v[174:177], v[112:127]
	v_mov_b32_e32 v204, v203
	v_cvt_pk_bf16_f32 v152, v128, v129
	v_cvt_pk_bf16_f32 v153, v130, v131
	v_cvt_pk_bf16_f32 v154, v132, v133
	v_cvt_pk_bf16_f32 v155, v134, v135
	v_cvt_pk_bf16_f32 v136, v136, v137
	v_cvt_pk_bf16_f32 v137, v138, v139
	v_cvt_pk_bf16_f32 v138, v140, v141
	v_cvt_pk_bf16_f32 v139, v142, v143
	v_cvt_pk_bf16_f32 v132, v144, v145
	v_cvt_pk_bf16_f32 v133, v146, v147
	v_cvt_pk_bf16_f32 v134, v148, v149
	v_cvt_pk_bf16_f32 v135, v150, v151
	v_cvt_pk_bf16_f32 v128, v242, v243
	v_cvt_pk_bf16_f32 v129, v244, v245
	v_cvt_pk_bf16_f32 v130, v156, v157
	v_cvt_pk_bf16_f32 v131, v158, v159
	s_nop 1
	v_permlane32_swap_b32_e32 v203, v204
	v_permlane32_swap_b32_e32 v152, v154
	v_permlane32_swap_b32_e32 v153, v155
	v_permlane32_swap_b32_e32 v136, v138
	v_permlane32_swap_b32_e32 v137, v139
	v_permlane32_swap_b32_e32 v132, v134
	v_permlane32_swap_b32_e32 v133, v135
	v_permlane32_swap_b32_e32 v128, v130
	v_permlane32_swap_b32_e32 v129, v131
	v_lshl_add_u32 v205, s30, 14, v221
	ds_read_b64_tr_b16 v[140:141], v205 offset:0
	ds_read_b64_tr_b16 v[142:143], v205 offset:0x800
	ds_read_b64_tr_b16 v[144:145], v205 offset:0x1000
	ds_read_b64_tr_b16 v[146:147], v205 offset:0x1800
	ds_read_b64_tr_b16 v[148:149], v205 offset:0x2000
	ds_read_b64_tr_b16 v[150:151], v205 offset:0x2800
	ds_read_b64_tr_b16 v[156:157], v205 offset:0x3000
	ds_read_b64_tr_b16 v[158:159], v205 offset:0x3800
	ds_read_b64_tr_b16 v[190:191], v205 offset:0x200
	ds_read_b64_tr_b16 v[192:193], v205 offset:0xa00
	ds_read_b64_tr_b16 v[208:209], v205 offset:0x1200
	ds_read_b64_tr_b16 v[210:211], v205 offset:0x1a00
	ds_read_b64_tr_b16 v[238:239], v205 offset:0x2200
	ds_read_b64_tr_b16 v[240:241], v205 offset:0x2a00
	ds_read_b64_tr_b16 v[242:243], v205 offset:0x3200
	ds_read_b64_tr_b16 v[244:245], v205 offset:0x3a00
	s_waitcnt lgkmcnt(8)
	s_nop 0
	v_mfma_f32_32x32x16_bf16 v[0:15], v[152:155], v[140:143], v[0:15]
	v_max_f32_e32 v140, v96, v97
	v_max3_f32 v140, v140, v112, v114
	v_max3_f32 v141, v98, v99, v113
	v_max3_f32 v140, v140, v115, v100
	v_max3_f32 v141, v141, v102, v103
	v_mfma_f32_32x32x16_bf16 v[0:15], v[136:139], v[144:147], v[0:15]
	v_max3_f32 v202, v140, v101, v116
	v_max3_f32 v246, v141, v118, v119
	v_mfma_f32_32x32x16_bf16 v[0:15], v[132:135], v[148:151], v[0:15]
	v_mfma_f32_32x32x16_bf16 v[0:15], v[128:131], v[156:159], v[0:15]
	ds_read_b64_tr_b16 v[156:157], v205 offset:0x400
	ds_read_b64_tr_b16 v[158:159], v205 offset:0xc00
	ds_read_b64_tr_b16 v[148:149], v205 offset:0x1400
	ds_read_b64_tr_b16 v[150:151], v205 offset:0x1c00
	ds_read_b64_tr_b16 v[144:145], v205 offset:0x2400
	ds_read_b64_tr_b16 v[146:147], v205 offset:0x2c00
	ds_read_b64_tr_b16 v[140:141], v205 offset:0x3400
	ds_read_b64_tr_b16 v[142:143], v205 offset:0x3c00
	s_waitcnt lgkmcnt(8)
	v_mfma_f32_32x32x16_bf16 v[48:63], v[152:155], v[190:193], v[48:63]
	v_max3_f32 v190, v202, v117, v104
	v_max3_f32 v191, v246, v106, v107
	v_max3_f32 v190, v190, v105, v120
	v_max3_f32 v191, v191, v122, v123
	v_max3_f32 v190, v190, v121, v108
	v_max3_f32 v191, v191, v110, v111
	v_max3_f32 v190, v190, v109, v124
	v_mfma_f32_32x32x16_bf16 v[48:63], v[136:139], v[208:211], v[48:63]
	v_max3_f32 v191, v191, v126, v127
	v_max3_f32 v190, v190, v125, v191
	v_mov_b32_e32 v191, v190
	s_nop 1
	v_permlane32_swap_b32_e32 v190, v191
	v_mfma_f32_32x32x16_bf16 v[48:63], v[132:135], v[238:241], v[48:63]
	v_max_f32_e32 v238, v190, v191
	v_mfma_f32_32x32x16_bf16 v[48:63], v[128:131], v[242:245], v[48:63]
	s_mov_b32 s2, 0x4138aa3b
	v_cmp_ge_f32_e32 vcc, s2, v238
	s_cmp_eq_u64 vcc, exec
	v_mov_b32_e32 v202, 1.0
	s_cbranch_scc0 .LBB0_860
